# coalesced output stores with nt hint
# baseline (speedup 1.0000x reference)
.LBB2_369:
	v_xor_b32_e32 v0, 1, v51
	v_add_u32_e32 v1, 64, v52
	v_cmp_lt_i32_e32 vcc, v0, v1
	s_waitcnt lgkmcnt(0)
	v_mul_f32_e32 v2, v53, v2
	v_cndmask_b32_e32 v0, v51, v0, vcc
	v_lshlrev_b32_e32 v65, 2, v0
	v_mul_f32_e32 v0, v53, v6
	s_nop 1
	v_mov_b32_dpp v1, v0 quad_perm:[1,0,3,2] row_mask:0xf bank_mask:0xf
	v_cmp_eq_u32_e32 vcc, 0, v44
	v_mul_f32_e32 v6, v53, v7
	s_nop 1
	v_mov_b32_dpp v7, v6 quad_perm:[1,0,3,2] row_mask:0xf bank_mask:0xf
	s_waitcnt lgkmcnt(1)
	v_cndmask_b32_e32 v52, v1, v0, vcc
	v_cndmask_b32_e32 v70, v0, v1, vcc
	v_mul_f32_e32 v0, v53, v8
	s_nop 1
	v_mov_b32_dpp v1, v0 quad_perm:[1,0,3,2] row_mask:0xf bank_mask:0xf
	s_nop 1
	v_mov_b32_dpp v8, v2 quad_perm:[1,0,3,2] row_mask:0xf bank_mask:0xf
	s_waitcnt lgkmcnt(2)
	v_cndmask_b32_e32 v54, v7, v6, vcc
	v_cndmask_b32_e32 v68, v6, v7, vcc
	v_mul_f32_e32 v6, v53, v9
	s_waitcnt lgkmcnt(1)
	v_cndmask_b32_e32 v56, v1, v0, vcc
	v_cndmask_b32_e32 v76, v0, v1, vcc
	v_mul_f32_e32 v0, v53, v3
	s_nop 1
	v_mov_b32_dpp v1, v0 quad_perm:[1,0,3,2] row_mask:0xf bank_mask:0xf
	s_waitcnt lgkmcnt(1)
	v_cndmask_b32_e32 v60, v8, v2, vcc
	v_cndmask_b32_e32 v72, v2, v8, vcc
	v_mul_f32_e32 v2, v53, v4
	v_mul_f32_e32 v4, v53, v5
	s_nop 1
	v_mov_b32_dpp v5, v4 quad_perm:[1,0,3,2] row_mask:0xf bank_mask:0xf
	s_nop 1
	v_mov_b32_dpp v3, v2 quad_perm:[1,0,3,2] row_mask:0xf bank_mask:0xf
	s_nop 1
	v_mov_b32_dpp v7, v6 quad_perm:[1,0,3,2] row_mask:0xf bank_mask:0xf
	s_waitcnt lgkmcnt(3)
	v_cndmask_b32_e32 v62, v1, v0, vcc
	v_cndmask_b32_e32 v82, v0, v1, vcc
	v_mul_u32_u24_e32 v0, 20, v44
	v_lshlrev_b32_e32 v66, 2, v0
	s_waitcnt lgkmcnt(2)
	v_cndmask_b32_e32 v84, v5, v4, vcc
	v_cndmask_b32_e32 v78, v4, v5, vcc
	v_add_u32_e32 v66, 0x16400, v66
	s_waitcnt lgkmcnt(1)
	v_cndmask_b32_e32 v86, v3, v2, vcc
	v_cndmask_b32_e32 v80, v2, v3, vcc
	ds_read_b128 v[48:51], v66 offset:6224
	ds_read_b128 v[88:91], v66 offset:6240
	ds_read_b128 v[32:35], v66 offset:6256
	ds_read_b128 v[16:19], v66 offset:6272
	ds_read_b128 v[0:3], v66 offset:6288
	ds_read_b128 v[92:95], v66
	ds_read_b128 v[96:99], v66 offset:16
	ds_read_b128 v[40:43], v66 offset:32
	s_waitcnt lgkmcnt(8)
	v_cndmask_b32_e32 v58, v7, v6, vcc
	v_cndmask_b32_e32 v74, v6, v7, vcc
	ds_read_b128 v[20:23], v66 offset:48
	ds_read_b128 v[4:7], v66 offset:64
	ds_read_b128 v[100:103], v66 offset:160
	ds_read_b128 v[104:107], v66 offset:176
	ds_read_b128 v[36:39], v66 offset:192
	ds_read_b128 v[24:27], v66 offset:208
	s_waitcnt vmcnt(0)
	ds_read_b128 v[8:11], v66 offset:224
	ds_read_b128 v[108:111], v66 offset:320
	ds_read_b128 v[112:115], v66 offset:336
	ds_read_b128 v[44:47], v66 offset:352
	ds_read_b128 v[28:31], v66 offset:368
	ds_read_b128 v[12:15], v66 offset:384
	s_waitcnt lgkmcnt(14)
	v_pk_fma_f32 v[48:49], v[52:53], v[92:93], v[48:49] op_sel_hi:[0,1,1]
	v_pk_fma_f32 v[50:51], v[52:53], v[94:95], v[50:51] op_sel_hi:[0,1,1]
	ds_read_b128 v[92:95], v66 offset:480
	ds_read_b128 v[116:119], v66 offset:496
	s_waitcnt lgkmcnt(11)
	v_pk_fma_f32 v[48:49], v[54:55], v[100:101], v[48:49] op_sel_hi:[0,1,1]
	v_pk_fma_f32 v[50:51], v[54:55], v[102:103], v[50:51] op_sel_hi:[0,1,1]
	ds_read_b128 v[120:123], v66 offset:512
	ds_read_b128 v[124:127], v66 offset:528
	s_waitcnt lgkmcnt(8)
	v_pk_fma_f32 v[100:101], v[56:57], v[108:109], v[48:49] op_sel_hi:[0,1,1]
	v_pk_fma_f32 v[102:103], v[56:57], v[110:111], v[50:51] op_sel_hi:[0,1,1]
	v_pk_fma_f32 v[96:97], v[52:53], v[96:97], v[88:89] op_sel_hi:[0,1,1]
	v_pk_fma_f32 v[108:109], v[52:53], v[98:99], v[90:91] op_sel_hi:[0,1,1]
	ds_read_b128 v[48:51], v66 offset:544
	ds_read_b128 v[88:91], v66 offset:640
	s_waitcnt lgkmcnt(5)
	v_pk_fma_f32 v[98:99], v[58:59], v[92:93], v[100:101] op_sel_hi:[0,1,1]
	v_pk_fma_f32 v[100:101], v[58:59], v[94:95], v[102:103] op_sel_hi:[0,1,1]
	ds_read_b128 v[92:95], v66 offset:800
	s_waitcnt lgkmcnt(1)
	v_pk_fma_f32 v[98:99], v[60:61], v[88:89], v[98:99] op_sel_hi:[0,1,1]
	v_pk_fma_f32 v[100:101], v[60:61], v[90:91], v[100:101] op_sel_hi:[0,1,1]
	ds_read_b128 v[88:91], v66 offset:816
	s_waitcnt lgkmcnt(1)
	v_pk_fma_f32 v[98:99], v[62:63], v[92:93], v[98:99] op_sel_hi:[0,1,1]
	v_pk_fma_f32 v[92:93], v[62:63], v[94:95], v[100:101] op_sel_hi:[0,1,1]
	v_pk_fma_f32 v[100:101], v[54:55], v[104:105], v[96:97] op_sel_hi:[0,1,1]
	v_pk_fma_f32 v[102:103], v[54:55], v[106:107], v[108:109] op_sel_hi:[0,1,1]
	ds_read_b128 v[94:97], v66 offset:656
	ds_read_b128 v[108:111], v66 offset:672
	v_pk_fma_f32 v[100:101], v[56:57], v[112:113], v[100:101] op_sel_hi:[0,1,1]
	v_pk_fma_f32 v[102:103], v[56:57], v[114:115], v[102:103] op_sel_hi:[0,1,1]
	v_pk_fma_f32 v[100:101], v[58:59], v[116:117], v[100:101] op_sel_hi:[0,1,1]
	v_pk_fma_f32 v[102:103], v[58:59], v[118:119], v[102:103] op_sel_hi:[0,1,1]
	ds_read_b128 v[112:115], v66 offset:688
	ds_read_b128 v[116:119], v66 offset:704
	v_pk_fma_f32 v[32:33], v[52:53], v[40:41], v[32:33] op_sel_hi:[0,1,1]
	v_pk_fma_f32 v[32:33], v[54:55], v[36:37], v[32:33] op_sel_hi:[0,1,1]
	v_pk_fma_f32 v[32:33], v[56:57], v[44:45], v[32:33] op_sel_hi:[0,1,1]
	s_waitcnt lgkmcnt(3)
	v_pk_fma_f32 v[94:95], v[60:61], v[94:95], v[100:101] op_sel_hi:[0,1,1]
	v_pk_fma_f32 v[32:33], v[58:59], v[120:121], v[32:33] op_sel_hi:[0,1,1]
	v_pk_fma_f32 v[106:107], v[62:63], v[88:89], v[94:95] op_sel_hi:[0,1,1]
	v_pk_fma_f32 v[88:89], v[60:61], v[96:97], v[102:103] op_sel_hi:[0,1,1]
	s_waitcnt lgkmcnt(2)
	v_pk_fma_f32 v[36:37], v[60:61], v[108:109], v[32:33] op_sel_hi:[0,1,1]
	v_pk_fma_f32 v[104:105], v[62:63], v[90:91], v[88:89] op_sel_hi:[0,1,1]
	ds_read_b128 v[88:91], v66 offset:832
	v_pk_fma_f32 v[40:41], v[52:53], v[42:43], v[34:35] op_sel_hi:[0,1,1]
	ds_read_b128 v[32:35], v66 offset:848
	v_pk_fma_f32 v[16:17], v[52:53], v[20:21], v[16:17] op_sel_hi:[0,1,1]
	v_pk_fma_f32 v[16:17], v[54:55], v[24:25], v[16:17] op_sel_hi:[0,1,1]
	v_pk_fma_f32 v[16:17], v[56:57], v[28:29], v[16:17] op_sel_hi:[0,1,1]
	v_pk_fma_f32 v[16:17], v[58:59], v[124:125], v[16:17] op_sel_hi:[0,1,1]
	s_waitcnt lgkmcnt(3)
	v_pk_fma_f32 v[16:17], v[60:61], v[112:113], v[16:17] op_sel_hi:[0,1,1]
	s_waitcnt lgkmcnt(1)
	v_pk_fma_f32 v[102:103], v[62:63], v[88:89], v[36:37] op_sel_hi:[0,1,1]
	s_waitcnt lgkmcnt(0)
	v_pk_fma_f32 v[88:89], v[62:63], v[32:33], v[16:17] op_sel_hi:[0,1,1]
	v_pk_fma_f32 v[16:17], v[52:53], v[22:23], v[18:19] op_sel_hi:[0,1,1]
	v_pk_fma_f32 v[16:17], v[54:55], v[26:27], v[16:17] op_sel_hi:[0,1,1]
	v_pk_fma_f32 v[16:17], v[56:57], v[30:31], v[16:17] op_sel_hi:[0,1,1]
	v_pk_fma_f32 v[16:17], v[58:59], v[126:127], v[16:17] op_sel_hi:[0,1,1]
	v_pk_fma_f32 v[16:17], v[60:61], v[114:115], v[16:17] op_sel_hi:[0,1,1]
	v_pk_fma_f32 v[94:95], v[62:63], v[34:35], v[16:17] op_sel_hi:[0,1,1]
	ds_read_b128 v[16:19], v66 offset:864
	v_pk_fma_f32 v[0:1], v[52:53], v[4:5], v[0:1] op_sel_hi:[0,1,1]
	v_pk_fma_f32 v[0:1], v[54:55], v[8:9], v[0:1] op_sel_hi:[0,1,1]
	v_pk_fma_f32 v[0:1], v[56:57], v[12:13], v[0:1] op_sel_hi:[0,1,1]
	v_pk_fma_f32 v[0:1], v[58:59], v[48:49], v[0:1] op_sel_hi:[0,1,1]
	v_pk_fma_f32 v[0:1], v[60:61], v[116:117], v[0:1] op_sel_hi:[0,1,1]
	ds_read_b128 v[32:35], v66 offset:960
	s_waitcnt lgkmcnt(1)
	v_pk_fma_f32 v[96:97], v[62:63], v[16:17], v[0:1] op_sel_hi:[0,1,1]
	v_pk_fma_f32 v[0:1], v[52:53], v[6:7], v[2:3] op_sel_hi:[0,1,1]
	v_pk_fma_f32 v[36:37], v[54:55], v[38:39], v[40:41] op_sel_hi:[0,1,1]
	v_pk_fma_f32 v[0:1], v[54:55], v[10:11], v[0:1] op_sel_hi:[0,1,1]
	v_pk_fma_f32 v[36:37], v[56:57], v[46:47], v[36:37] op_sel_hi:[0,1,1]
	v_pk_fma_f32 v[0:1], v[56:57], v[14:15], v[0:1] op_sel_hi:[0,1,1]
	v_pk_fma_f32 v[36:37], v[58:59], v[122:123], v[36:37] op_sel_hi:[0,1,1]
	v_pk_fma_f32 v[0:1], v[58:59], v[50:51], v[0:1] op_sel_hi:[0,1,1]
	v_pk_fma_f32 v[36:37], v[60:61], v[110:111], v[36:37] op_sel_hi:[0,1,1]
	v_pk_fma_f32 v[0:1], v[60:61], v[118:119], v[0:1] op_sel_hi:[0,1,1]
	v_pk_fma_f32 v[100:101], v[62:63], v[90:91], v[36:37] op_sel_hi:[0,1,1]
	v_pk_fma_f32 v[90:91], v[62:63], v[18:19], v[0:1] op_sel_hi:[0,1,1]
	ds_read_b128 v[48:51], v66 offset:976
	ds_read_b128 v[28:31], v66 offset:992
	ds_read_b128 v[16:19], v66 offset:1008
	ds_read_b128 v[0:3], v66 offset:1024
	ds_read_b128 v[44:47], v66 offset:1120
	ds_read_b128 v[52:55], v66 offset:1136
	ds_read_b128 v[36:39], v66 offset:1152
	ds_read_b128 v[20:23], v66 offset:1168
	ds_read_b128 v[4:7], v66 offset:1184
	ds_read_b128 v[108:111], v66 offset:1280
	ds_read_b128 v[56:59], v66 offset:1296
	ds_read_b128 v[40:43], v66 offset:1312
	ds_read_b128 v[24:27], v66 offset:1328
	ds_read_b128 v[8:11], v66 offset:1344
	ds_read_b128 v[112:115], v66 offset:1440
	ds_read_b128 v[60:63], v66 offset:1456
	ds_read_b128 v[12:15], v66 offset:1504
	ds_read_b128 v[116:119], v66 offset:1600
	s_waitcnt lgkmcnt(14)
	v_pk_fma_f32 v[32:33], v[86:87], v[32:33], v[98:99] op_sel_hi:[0,1,1]
	v_pk_fma_f32 v[34:35], v[86:87], v[34:35], v[92:93] op_sel_hi:[0,1,1]
	s_waitcnt lgkmcnt(13)
	v_pk_fma_f32 v[32:33], v[84:85], v[44:45], v[32:33] op_sel_hi:[0,1,1]
	v_pk_fma_f32 v[34:35], v[84:85], v[46:47], v[34:35] op_sel_hi:[0,1,1]
	ds_read_b128 v[120:123], v66 offset:1760
	ds_read_b128 v[124:127], v66 offset:1776
	s_waitcnt lgkmcnt(10)
	v_pk_fma_f32 v[92:93], v[70:71], v[108:109], v[32:33] op_sel_hi:[0,1,1]
	v_pk_fma_f32 v[98:99], v[70:71], v[110:111], v[34:35] op_sel_hi:[0,1,1]
	ds_read_b128 v[32:35], v66 offset:1824
	ds_read_b128 v[44:47], v66 offset:1920
	s_waitcnt lgkmcnt(7)
	v_pk_fma_f32 v[92:93], v[68:69], v[112:113], v[92:93] op_sel_hi:[0,1,1]
	v_pk_fma_f32 v[98:99], v[68:69], v[114:115], v[98:99] op_sel_hi:[0,1,1]
	ds_read_b128 v[108:111], v66 offset:2080
	ds_read_b128 v[112:115], v66 offset:2096
	s_waitcnt lgkmcnt(6)
	v_pk_fma_f32 v[92:93], v[76:77], v[116:117], v[92:93] op_sel_hi:[0,1,1]
	v_pk_fma_f32 v[98:99], v[76:77], v[118:119], v[98:99] op_sel_hi:[0,1,1]
	s_waitcnt lgkmcnt(5)
	v_pk_fma_f32 v[92:93], v[74:75], v[120:121], v[92:93] op_sel_hi:[0,1,1]
	v_pk_fma_f32 v[98:99], v[74:75], v[122:123], v[98:99] op_sel_hi:[0,1,1]
	s_waitcnt lgkmcnt(2)
	v_pk_fma_f32 v[92:93], v[72:73], v[44:45], v[92:93] op_sel_hi:[0,1,1]
	v_pk_fma_f32 v[98:99], v[72:73], v[46:47], v[98:99] op_sel_hi:[0,1,1]
	ds_read_b128 v[44:47], v66 offset:2144
	ds_read_b128 v[116:119], v66 offset:2240
	s_waitcnt lgkmcnt(3)
	v_pk_fma_f32 v[92:93], v[82:83], v[108:109], v[92:93] op_sel_hi:[0,1,1]
	v_pk_fma_f32 v[98:99], v[82:83], v[110:111], v[98:99] op_sel_hi:[0,1,1]
	ds_read_b128 v[108:111], v66 offset:2400
	s_waitcnt lgkmcnt(1)
	v_pk_fma_f32 v[92:93], v[80:81], v[116:117], v[92:93] op_sel_hi:[0,1,1]
	v_pk_fma_f32 v[98:99], v[80:81], v[118:119], v[98:99] op_sel_hi:[0,1,1]
	s_waitcnt lgkmcnt(0)
	v_pk_fma_f32 v[92:93], v[78:79], v[108:109], v[92:93] op_sel_hi:[0,1,1]
	v_pk_fma_f32 v[98:99], v[78:79], v[110:111], v[98:99] op_sel_hi:[0,1,1]
	v_pk_fma_f32 v[108:109], v[86:87], v[48:49], v[106:107] op_sel_hi:[0,1,1]
	v_pk_fma_f32 v[110:111], v[86:87], v[50:51], v[104:105] op_sel_hi:[0,1,1]
	ds_read_b128 v[116:119], v66 offset:2416
	ds_read_b128 v[104:107], v66 offset:1472
	ds_read_b128 v[48:51], v66 offset:1488
	v_pk_fma_f32 v[52:53], v[84:85], v[52:53], v[108:109] op_sel_hi:[0,1,1]
	v_pk_fma_f32 v[54:55], v[84:85], v[54:55], v[110:111] op_sel_hi:[0,1,1]
	v_pk_fma_f32 v[56:57], v[70:71], v[56:57], v[52:53] op_sel_hi:[0,1,1]
	v_pk_fma_f32 v[58:59], v[70:71], v[58:59], v[54:55] op_sel_hi:[0,1,1]
	ds_read_b128 v[52:55], v66 offset:1616
	ds_read_b128 v[108:111], v66 offset:1632
	v_pk_fma_f32 v[56:57], v[68:69], v[60:61], v[56:57] op_sel_hi:[0,1,1]
	v_pk_fma_f32 v[58:59], v[68:69], v[62:63], v[58:59] op_sel_hi:[0,1,1]
	s_waitcnt lgkmcnt(1)
	v_pk_fma_f32 v[56:57], v[76:77], v[52:53], v[56:57] op_sel_hi:[0,1,1]
	v_pk_fma_f32 v[58:59], v[76:77], v[54:55], v[58:59] op_sel_hi:[0,1,1]
	ds_read_b128 v[52:55], v66 offset:1936
	v_pk_fma_f32 v[56:57], v[74:75], v[124:125], v[56:57] op_sel_hi:[0,1,1]
	v_pk_fma_f32 v[58:59], v[74:75], v[126:127], v[58:59] op_sel_hi:[0,1,1]
	ds_read_b128 v[60:63], v66 offset:1952
	s_waitcnt lgkmcnt(1)
	v_pk_fma_f32 v[56:57], v[72:73], v[52:53], v[56:57] op_sel_hi:[0,1,1]
	v_pk_fma_f32 v[58:59], v[72:73], v[54:55], v[58:59] op_sel_hi:[0,1,1]
	ds_read_b128 v[52:55], v66 offset:2256
	v_pk_fma_f32 v[56:57], v[82:83], v[112:113], v[56:57] op_sel_hi:[0,1,1]
	v_pk_fma_f32 v[58:59], v[82:83], v[114:115], v[58:59] op_sel_hi:[0,1,1]
	s_waitcnt lgkmcnt(0)
	v_pk_fma_f32 v[56:57], v[80:81], v[52:53], v[56:57] op_sel_hi:[0,1,1]
	v_pk_fma_f32 v[58:59], v[80:81], v[54:55], v[58:59] op_sel_hi:[0,1,1]
	v_pk_fma_f32 v[56:57], v[78:79], v[116:117], v[56:57] op_sel_hi:[0,1,1]
	v_pk_fma_f32 v[58:59], v[78:79], v[118:119], v[58:59] op_sel_hi:[0,1,1]
	v_pk_fma_f32 v[116:117], v[86:87], v[28:29], v[102:103] op_sel_hi:[0,1,1]
	v_pk_fma_f32 v[118:119], v[86:87], v[30:31], v[100:101] op_sel_hi:[0,1,1]
	ds_read_b128 v[112:115], v66 offset:2272
	ds_read_b128 v[120:123], v66 offset:1648
	ds_read_b128 v[52:55], v66 offset:1664
	v_pk_fma_f32 v[36:37], v[84:85], v[36:37], v[116:117] op_sel_hi:[0,1,1]
	v_pk_fma_f32 v[38:39], v[84:85], v[38:39], v[118:119] op_sel_hi:[0,1,1]
	ds_read_b128 v[28:31], v66 offset:1792
	ds_read_b128 v[100:103], v66 offset:1808
	v_pk_fma_f32 v[116:117], v[70:71], v[40:41], v[36:37] op_sel_hi:[0,1,1]
	v_pk_fma_f32 v[118:119], v[70:71], v[42:43], v[38:39] op_sel_hi:[0,1,1]
	ds_read_b128 v[36:39], v66 offset:1968
	ds_read_b128 v[40:43], v66 offset:1984
	v_pk_fma_f32 v[104:105], v[68:69], v[104:105], v[116:117] op_sel_hi:[0,1,1]
	v_pk_fma_f32 v[106:107], v[68:69], v[106:107], v[118:119] op_sel_hi:[0,1,1]
	v_pk_fma_f32 v[116:117], v[76:77], v[108:109], v[104:105] op_sel_hi:[0,1,1]
	v_pk_fma_f32 v[118:119], v[76:77], v[110:111], v[106:107] op_sel_hi:[0,1,1]
	ds_read_b128 v[104:107], v66 offset:2112
	ds_read_b128 v[108:111], v66 offset:2128
	s_waitcnt lgkmcnt(5)
	v_pk_fma_f32 v[28:29], v[74:75], v[28:29], v[116:117] op_sel_hi:[0,1,1]
	v_pk_fma_f32 v[30:31], v[74:75], v[30:31], v[118:119] op_sel_hi:[0,1,1]
	v_pk_fma_f32 v[16:17], v[86:87], v[16:17], v[88:89] op_sel_hi:[0,1,1]
	v_pk_fma_f32 v[28:29], v[72:73], v[60:61], v[28:29] op_sel_hi:[0,1,1]
	v_pk_fma_f32 v[30:31], v[72:73], v[62:63], v[30:31] op_sel_hi:[0,1,1]
	ds_read_b128 v[60:63], v66 offset:2288
	ds_read_b128 v[116:119], v66 offset:2304
	v_pk_fma_f32 v[16:17], v[84:85], v[20:21], v[16:17] op_sel_hi:[0,1,1]
	v_pk_fma_f32 v[18:19], v[86:87], v[18:19], v[94:95] op_sel_hi:[0,1,1]
	s_waitcnt lgkmcnt(3)
	v_pk_fma_f32 v[104:105], v[82:83], v[104:105], v[28:29] op_sel_hi:[0,1,1]
	v_pk_fma_f32 v[106:107], v[82:83], v[106:107], v[30:31] op_sel_hi:[0,1,1]
	ds_read_b128 v[28:31], v66 offset:2432
	v_pk_fma_f32 v[16:17], v[70:71], v[24:25], v[16:17] op_sel_hi:[0,1,1]
	v_pk_fma_f32 v[18:19], v[84:85], v[22:23], v[18:19] op_sel_hi:[0,1,1]
	v_pk_fma_f32 v[0:1], v[86:87], v[0:1], v[96:97] op_sel_hi:[0,1,1]
	v_pk_fma_f32 v[16:17], v[68:69], v[48:49], v[16:17] op_sel_hi:[0,1,1]
	v_pk_fma_f32 v[18:19], v[70:71], v[26:27], v[18:19] op_sel_hi:[0,1,1]
	ds_read_b128 v[20:23], v66 offset:2464
	v_pk_fma_f32 v[0:1], v[84:85], v[4:5], v[0:1] op_sel_hi:[0,1,1]
	v_pk_fma_f32 v[2:3], v[86:87], v[2:3], v[90:91] op_sel_hi:[0,1,1]
	v_pk_fma_f32 v[112:113], v[80:81], v[112:113], v[104:105] op_sel_hi:[0,1,1]
	v_pk_fma_f32 v[114:115], v[80:81], v[114:115], v[106:107] op_sel_hi:[0,1,1]
	ds_read_b128 v[104:107], v66 offset:2448
	v_subrev_u32_e32 v66, 0x16400, v66
	v_pk_fma_f32 v[16:17], v[76:77], v[120:121], v[16:17] op_sel_hi:[0,1,1]
	v_pk_fma_f32 v[18:19], v[68:69], v[50:51], v[18:19] op_sel_hi:[0,1,1]
	v_pk_fma_f32 v[0:1], v[70:71], v[8:9], v[0:1] op_sel_hi:[0,1,1]
	v_pk_fma_f32 v[2:3], v[84:85], v[6:7], v[2:3] op_sel_hi:[0,1,1]
	v_max_f32_e32 v4, v92, v93
	v_pk_fma_f32 v[16:17], v[74:75], v[100:101], v[16:17] op_sel_hi:[0,1,1]
	v_pk_fma_f32 v[18:19], v[76:77], v[122:123], v[18:19] op_sel_hi:[0,1,1]
	v_pk_fma_f32 v[0:1], v[68:69], v[12:13], v[0:1] op_sel_hi:[0,1,1]
	v_pk_fma_f32 v[2:3], v[70:71], v[10:11], v[2:3] op_sel_hi:[0,1,1]
	v_max3_f32 v4, v4, v98, v99
	v_pk_fma_f32 v[16:17], v[72:73], v[36:37], v[16:17] op_sel_hi:[0,1,1]
	v_pk_fma_f32 v[18:19], v[74:75], v[102:103], v[18:19] op_sel_hi:[0,1,1]
	v_pk_fma_f32 v[0:1], v[76:77], v[52:53], v[0:1] op_sel_hi:[0,1,1]
	v_pk_fma_f32 v[2:3], v[68:69], v[14:15], v[2:3] op_sel_hi:[0,1,1]
	v_max3_f32 v4, v4, v56, v57
	s_waitcnt lgkmcnt(2)
	v_pk_fma_f32 v[28:29], v[78:79], v[28:29], v[112:113] op_sel_hi:[0,1,1]
	v_pk_fma_f32 v[16:17], v[82:83], v[108:109], v[16:17] op_sel_hi:[0,1,1]
	v_pk_fma_f32 v[18:19], v[72:73], v[38:39], v[18:19] op_sel_hi:[0,1,1]
	v_pk_fma_f32 v[0:1], v[74:75], v[32:33], v[0:1] op_sel_hi:[0,1,1]
	v_pk_fma_f32 v[2:3], v[76:77], v[54:55], v[2:3] op_sel_hi:[0,1,1]
	v_max3_f32 v4, v4, v58, v59
	v_pk_fma_f32 v[30:31], v[78:79], v[30:31], v[114:115] op_sel_hi:[0,1,1]
	v_pk_fma_f32 v[16:17], v[80:81], v[60:61], v[16:17] op_sel_hi:[0,1,1]
	v_pk_fma_f32 v[18:19], v[82:83], v[110:111], v[18:19] op_sel_hi:[0,1,1]
	v_pk_fma_f32 v[0:1], v[72:73], v[40:41], v[0:1] op_sel_hi:[0,1,1]
	v_pk_fma_f32 v[2:3], v[74:75], v[34:35], v[2:3] op_sel_hi:[0,1,1]
	v_max3_f32 v4, v4, v28, v29
	s_waitcnt lgkmcnt(0)
	v_pk_fma_f32 v[16:17], v[78:79], v[104:105], v[16:17] op_sel_hi:[0,1,1]
	v_pk_fma_f32 v[18:19], v[80:81], v[62:63], v[18:19] op_sel_hi:[0,1,1]
	v_pk_fma_f32 v[0:1], v[82:83], v[44:45], v[0:1] op_sel_hi:[0,1,1]
	v_pk_fma_f32 v[2:3], v[72:73], v[42:43], v[2:3] op_sel_hi:[0,1,1]
	v_max3_f32 v4, v4, v30, v31
	v_pk_fma_f32 v[18:19], v[78:79], v[106:107], v[18:19] op_sel_hi:[0,1,1]
	v_pk_fma_f32 v[0:1], v[80:81], v[116:117], v[0:1] op_sel_hi:[0,1,1]
	v_pk_fma_f32 v[2:3], v[82:83], v[46:47], v[2:3] op_sel_hi:[0,1,1]
	v_max3_f32 v4, v4, v16, v17
	v_pk_fma_f32 v[0:1], v[78:79], v[20:21], v[0:1] op_sel_hi:[0,1,1]
	v_pk_fma_f32 v[2:3], v[80:81], v[118:119], v[2:3] op_sel_hi:[0,1,1]
	v_max3_f32 v4, v4, v18, v19
	v_pk_fma_f32 v[2:3], v[78:79], v[22:23], v[2:3] op_sel_hi:[0,1,1]
	v_max3_f32 v4, v4, v0, v1
	v_max3_f32 v4, v4, v2, v3
	s_nop 1
	v_mov_b32_dpp v5, v4 quad_perm:[1,0,3,2] row_mask:0xf bank_mask:0xf
	s_waitcnt lgkmcnt(0)
	v_max_f32_e32 v5, v5, v5
	v_max_f32_e32 v4, v4, v5
	v_sub_f32_e32 v5, v92, v4
	v_mul_f32_e32 v5, 0x3fb8aa3b, v5
	v_sub_f32_e32 v6, v93, v4
	v_exp_f32_e32 v5, v5
	v_mul_f32_e32 v6, 0x3fb8aa3b, v6
	v_sub_f32_e32 v7, v98, v4
	v_exp_f32_e32 v6, v6
	v_mul_f32_e32 v7, 0x3fb8aa3b, v7
	v_sub_f32_e32 v8, v99, v4
	v_exp_f32_e32 v7, v7
	v_mul_f32_e32 v8, 0x3fb8aa3b, v8
	v_exp_f32_e32 v8, v8
	v_add_f32_e32 v5, 0, v5
	v_add_f32_e32 v5, v5, v6
	v_sub_f32_e32 v6, v56, v4
	v_add_f32_e32 v5, v5, v7
	v_mul_f32_e32 v6, 0x3fb8aa3b, v6
	v_sub_f32_e32 v7, v57, v4
	v_add_f32_e32 v5, v5, v8
	v_exp_f32_e32 v6, v6
	v_mul_f32_e32 v7, 0x3fb8aa3b, v7
	v_sub_f32_e32 v8, v58, v4
	v_exp_f32_e32 v7, v7
	v_mul_f32_e32 v8, 0x3fb8aa3b, v8
	v_sub_f32_e32 v9, v59, v4
	v_exp_f32_e32 v8, v8
	v_mul_f32_e32 v9, 0x3fb8aa3b, v9
	v_exp_f32_e32 v9, v9
	v_add_f32_e32 v5, v5, v6
	v_sub_f32_e32 v6, v28, v4
	v_add_f32_e32 v5, v5, v7
	v_mul_f32_e32 v6, 0x3fb8aa3b, v6
	v_sub_f32_e32 v7, v29, v4
	v_add_f32_e32 v5, v5, v8
	v_exp_f32_e32 v6, v6
	v_mul_f32_e32 v7, 0x3fb8aa3b, v7
	v_sub_f32_e32 v8, v30, v4
	v_add_f32_e32 v5, v5, v9
	v_exp_f32_e32 v7, v7
	v_mul_f32_e32 v8, 0x3fb8aa3b, v8
	v_sub_f32_e32 v9, v31, v4
	v_exp_f32_e32 v8, v8
	v_mul_f32_e32 v9, 0x3fb8aa3b, v9
	v_exp_f32_e32 v9, v9
	v_add_f32_e32 v5, v5, v6
	v_sub_f32_e32 v6, v16, v4
	v_add_f32_e32 v5, v5, v7
	v_mul_f32_e32 v6, 0x3fb8aa3b, v6
	v_sub_f32_e32 v7, v17, v4
	v_add_f32_e32 v5, v5, v8
	v_exp_f32_e32 v6, v6
	v_mul_f32_e32 v7, 0x3fb8aa3b, v7
	v_sub_f32_e32 v8, v18, v4
	v_add_f32_e32 v5, v5, v9
	v_exp_f32_e32 v7, v7
	v_mul_f32_e32 v8, 0x3fb8aa3b, v8
	v_sub_f32_e32 v9, v19, v4
	v_exp_f32_e32 v8, v8
	v_mul_f32_e32 v9, 0x3fb8aa3b, v9
	v_exp_f32_e32 v9, v9
	v_add_f32_e32 v5, v5, v6
	v_sub_f32_e32 v6, v0, v4
	v_add_f32_e32 v5, v5, v7
	v_mul_f32_e32 v6, 0x3fb8aa3b, v6
	v_sub_f32_e32 v7, v1, v4
	v_add_f32_e32 v5, v5, v8
	v_exp_f32_e32 v6, v6
	v_mul_f32_e32 v7, 0x3fb8aa3b, v7
	v_sub_f32_e32 v8, v2, v4
	v_add_f32_e32 v5, v5, v9
	v_exp_f32_e32 v7, v7
	v_mul_f32_e32 v8, 0x3fb8aa3b, v8
	v_sub_f32_e32 v9, v3, v4
	v_exp_f32_e32 v8, v8
	v_mul_f32_e32 v9, 0x3fb8aa3b, v9
	v_exp_f32_e32 v9, v9
	v_add_f32_e32 v5, v5, v6
	v_add_f32_e32 v5, v5, v7
	v_add_f32_e32 v5, v5, v8
	v_add_f32_e32 v5, v5, v9
	s_nop 1
	v_mov_b32_dpp v6, v5 quad_perm:[1,0,3,2] row_mask:0xf bank_mask:0xf
	s_and_b64 exec, exec, s[8:9]
	s_cbranch_execz .LBB2_371
	s_waitcnt lgkmcnt(0)
	v_add_f32_e32 v5, v5, v6
	s_mov_b32 s0, 0x800000
	v_cmp_gt_f32_e32 vcc, s0, v5
	s_mov_b32 s0, 0x3f317217
	v_mov_b32_e32 v67, 0
	v_cndmask_b32_e64 v6, 0, 32, vcc
	v_ldexp_f32 v5, v5, v6
	v_log_f32_e32 v5, v5
	s_nop 0
	v_mul_f32_e32 v6, 0x3f317217, v5
	v_fma_f32 v6, v5, s0, -v6
	v_fmamk_f32 v6, v5, 0x3377d1cf, v6
	s_mov_b32 s0, 0x7f800000
	v_fmac_f32_e32 v6, 0x3f317217, v5
	v_cmp_lt_f32_e64 s[0:1], |v5|, s0
	s_nop 1
	v_cndmask_b32_e64 v5, v5, v6, s[0:1]
	v_mov_b32_e32 v6, 0x41b17218
	v_cndmask_b32_e32 v6, 0, v6, vcc
	v_sub_f32_e32 v5, v5, v6
	v_add_f32_e32 v10, v4, v5
	s_mov_b64 s[0:1], exec
	s_bcnt1_i32_b64 s94, exec
	s_mulk_i32 s94, 0x50
	s_lshl_b32 s92, s91, 5
	s_add_i32 s92, s92, s64
	s_mulk_i32 s92, 0xa0
	s_add_u32 s92, s52, s92
	s_addc_u32 s93, s53, 0
	s_mul_i32 s95, s91, 0x1400
	s_add_i32 s90, s95, 0x11940
	s_add_i32 s95, s95, 0x10000
	s_cmp_lt_u32 s91, 5
	s_cselect_b32 s95, s95, s90
	v_mbcnt_lo_u32_b32 v9, -1, 0
	v_mbcnt_hi_u32_b32 v9, -1, v9
	v_mul_u32_u24_e32 v8, 0x50, v9
	v_add_u32_e32 v8, s95, v8
	v_sub_f32_e32 v7, v99, v10
	v_sub_f32_e32 v6, v98, v10
	v_sub_f32_e32 v5, v93, v10
	v_sub_f32_e32 v4, v92, v10
	ds_write_b128 v8, v[4:7]
	v_sub_f32_e32 v3, v3, v10
	v_sub_f32_e32 v2, v2, v10
	v_sub_f32_e32 v7, v59, v10
	v_sub_f32_e32 v6, v58, v10
	v_sub_f32_e32 v5, v57, v10
	v_sub_f32_e32 v4, v56, v10
	ds_write_b128 v8, v[4:7] offset:16
	v_sub_f32_e32 v1, v1, v10
	v_sub_f32_e32 v0, v0, v10
	v_sub_f32_e32 v7, v31, v10
	v_sub_f32_e32 v6, v30, v10
	v_sub_f32_e32 v5, v29, v10
	v_sub_f32_e32 v4, v28, v10
	ds_write_b128 v8, v[4:7] offset:32
	ds_write_b128 v8, v[0:3] offset:64
	v_sub_f32_e32 v7, v19, v10
	v_sub_f32_e32 v6, v18, v10
	v_sub_f32_e32 v5, v17, v10
	v_sub_f32_e32 v4, v16, v10
	ds_write_b128 v8, v[4:7] offset:48
	s_mov_b64 exec, -1
	v_mbcnt_lo_u32_b32 v9, -1, 0
	v_mbcnt_hi_u32_b32 v9, -1, v9
	v_lshlrev_b32_e32 v9, 4, v9
	v_add_u32_e32 v8, s95, v9
	v_add_u32_e32 v11, 0x1000, v9
	s_waitcnt lgkmcnt(0)
	ds_read_b128 v[12:15], v8
	ds_read_b128 v[16:19], v8 offset:1024
	ds_read_b128 v[20:23], v8 offset:2048
	ds_read_b128 v[24:27], v8 offset:3072
	ds_read_b128 v[28:31], v8 offset:4096
	v_cmp_gt_i32_e32 vcc, s94, v9
	s_mov_b64 exec, vcc
	s_waitcnt lgkmcnt(4)
	global_store_dwordx4 v9, v[12:15], s[92:93] nt
	s_sub_i32 s94, s94, 0x400
	v_cmp_gt_i32_e32 vcc, s94, v9
	s_mov_b64 exec, vcc
	s_waitcnt lgkmcnt(3)
	global_store_dwordx4 v9, v[16:19], s[92:93] offset:1024 nt
	s_sub_i32 s94, s94, 0x400
	v_cmp_gt_i32_e32 vcc, s94, v9
	s_mov_b64 exec, vcc
	s_waitcnt lgkmcnt(2)
	global_store_dwordx4 v9, v[20:23], s[92:93] offset:2048 nt
	s_sub_i32 s94, s94, 0x400
	v_cmp_gt_i32_e32 vcc, s94, v9
	s_mov_b64 exec, vcc
	s_waitcnt lgkmcnt(1)
	global_store_dwordx4 v9, v[24:27], s[92:93] offset:3072 nt
	s_sub_i32 s94, s94, 0x400
	v_cmp_gt_i32_e32 vcc, s94, v9
	s_mov_b64 exec, vcc
	s_waitcnt lgkmcnt(0)
	global_store_dwordx4 v11, v[28:31], s[92:93] nt
